# MLA row sums on 2-pass 4x4x4 bf16 MFMAs (ones x own P values, per-lane sum) instead of VALU dot2c: 8 short MFMAs per 64-key tile, four accumulator quads in rotation
# speedup vs baseline: 1.0111x; 1.0052x over previous
.LBB0_1539:
	v_exp_f32_e32 v36, v116
	v_exp_f32_e32 v40, v132
	v_exp_f32_e32 v37, v117
	v_exp_f32_e32 v41, v133
	v_exp_f32_e32 v38, v118
	v_exp_f32_e32 v42, v134
	v_exp_f32_e32 v39, v119
	v_exp_f32_e32 v43, v135
	v_exp_f32_e32 v44, v120
	v_exp_f32_e32 v45, v136
	v_exp_f32_e32 v46, v121
	v_exp_f32_e32 v47, v137
	v_exp_f32_e32 v48, v122
	v_exp_f32_e32 v49, v138
	v_exp_f32_e32 v50, v123
	v_exp_f32_e32 v51, v139
	v_exp_f32_e32 v52, v124
	v_exp_f32_e32 v53, v140
	v_exp_f32_e32 v54, v125
	v_exp_f32_e32 v55, v141
	v_exp_f32_e32 v56, v126
	v_exp_f32_e32 v57, v142
	v_exp_f32_e32 v58, v127
	v_exp_f32_e32 v59, v143
	v_exp_f32_e32 v60, v128
	v_exp_f32_e32 v61, v144
	v_exp_f32_e32 v62, v129
	v_exp_f32_e32 v63, v145
	v_exp_f32_e32 v64, v130
	v_exp_f32_e32 v65, v146
	v_exp_f32_e32 v66, v131
	v_exp_f32_e32 v68, v147
	v_cvt_pk_bf16_f32 v36, v36, v37
	v_cvt_pk_bf16_f32 v37, v38, v39
	v_cvt_pk_bf16_f32 v38, v44, v46
	v_cvt_pk_bf16_f32 v39, v48, v50
	v_cvt_pk_bf16_f32 v40, v40, v41
	v_cvt_pk_bf16_f32 v41, v42, v43
	v_cvt_pk_bf16_f32 v42, v45, v47
	v_cvt_pk_bf16_f32 v43, v49, v51
	v_cvt_pk_bf16_f32 v44, v52, v54
	v_cvt_pk_bf16_f32 v45, v56, v58
	v_cvt_pk_bf16_f32 v46, v60, v62
	v_cvt_pk_bf16_f32 v47, v64, v66
	v_cvt_pk_bf16_f32 v48, v53, v55
	v_cvt_pk_bf16_f32 v49, v57, v59
	v_cvt_pk_bf16_f32 v50, v61, v63
	v_cvt_pk_bf16_f32 v51, v65, v68
	v_mov_b64_e32 v[52:53], s[92:93]
	v_mov_b64_e32 v[54:55], s[94:95]
	ds_read_b64_tr_b16 v[56:57], v205 offset:0
	ds_read_b64_tr_b16 v[58:59], v205 offset:1024
	ds_read_b64_tr_b16 v[60:61], v67 offset:0
	ds_read_b64_tr_b16 v[62:63], v67 offset:1024
	s_nop 1
	v_mfma_f32_4x4x4_16b_bf16 v[100:103], v[52:53], v[36:37], v[100:103]
	v_mfma_f32_4x4x4_16b_bf16 v[104:107], v[52:53], v[38:39], v[104:107]
	v_mfma_f32_4x4x4_16b_bf16 v[108:111], v[52:53], v[44:45], v[108:111]
	v_mfma_f32_4x4x4_16b_bf16 v[112:115], v[52:53], v[46:47], v[112:115]
	v_mfma_f32_4x4x4_16b_bf16 v[100:103], v[52:53], v[40:41], v[100:103]
	v_mfma_f32_4x4x4_16b_bf16 v[104:107], v[52:53], v[42:43], v[104:107]
	v_mfma_f32_4x4x4_16b_bf16 v[108:111], v[52:53], v[48:49], v[108:111]
	v_mfma_f32_4x4x4_16b_bf16 v[112:115], v[52:53], v[50:51], v[112:115]
	ds_read_b64_tr_b16 v[52:53], v205 offset:2048
	ds_read_b64_tr_b16 v[54:55], v205 offset:3072
	ds_read_b64_tr_b16 v[68:69], v67 offset:2048
	ds_read_b64_tr_b16 v[70:71], v67 offset:3072
	s_nop 0
	s_waitcnt lgkmcnt(0)
	s_nop 0
	v_mfma_f32_32x32x16_bf16 v[2:17], v[56:59], v[36:39], v[2:17]
	v_mfma_f32_32x32x16_bf16 v[18:33], v[60:63], v[36:39], v[18:33]
	ds_read_b64_tr_b16 v[36:37], v205 offset:4096
	ds_read_b64_tr_b16 v[38:39], v205 offset:5120
	v_mfma_f32_32x32x16_bf16 v[2:17], v[52:55], v[44:47], v[2:17]
	v_mfma_f32_32x32x16_bf16 v[18:33], v[68:71], v[44:47], v[18:33]
	ds_read_b64_tr_b16 v[44:45], v67 offset:4096
	ds_read_b64_tr_b16 v[46:47], v67 offset:5120
	ds_read_b64_tr_b16 v[52:53], v205 offset:6144
	ds_read_b64_tr_b16 v[54:55], v205 offset:7168
	ds_read_b64_tr_b16 v[56:57], v67 offset:6144
	ds_read_b64_tr_b16 v[58:59], v67 offset:7168
	s_nop 0
	s_waitcnt lgkmcnt(0)
	s_nop 0
	v_mfma_f32_32x32x16_bf16 v[2:17], v[36:39], v[40:43], v[2:17]
	v_mfma_f32_32x32x16_bf16 v[18:33], v[44:47], v[40:43], v[18:33]
	v_mfma_f32_32x32x16_bf16 v[2:17], v[52:55], v[48:51], v[2:17]
	v_mfma_f32_32x32x16_bf16 v[18:33], v[56:59], v[48:51], v[18:33]
	s_setprio 0
	v_add_f32_e32 v34, v100, v104
	v_add_f32_e32 v38, v108, v112
	v_add_f32_e32 v34, v34, v38
	v_mov_b32_e32 v38, v34
	s_nop 1
	v_permlane32_swap_b32_e32 v34, v38
	v_add_f32_e32 v34, v34, v38
	v_div_scale_f32 v38, s[2:3], v34, v34, 1.0
	v_rcp_f32_e32 v39, v38
	v_lshlrev_b64 v[36:37], 11, v[172:173]
	v_lshl_add_u64 v[36:37], s[52:53], 0, v[36:37]
	s_lshl_b32 s4, s12, 1
	v_fma_f32 v40, -v38, v39, 1.0
	v_fmac_f32_e32 v39, v40, v39
	v_div_scale_f32 v40, vcc, 1.0, v34, 1.0
	v_mul_f32_e32 v41, v40, v39
	v_fma_f32 v42, -v38, v41, v40
	v_fmac_f32_e32 v41, v42, v39
	v_fma_f32 v38, -v38, v41, v40
	v_div_fmas_f32 v38, v38, v39, v41
	v_div_fixup_f32 v34, v38, v34, 1.0
	v_pk_mul_f32 v[2:3], v[2:3], v[34:35] op_sel_hi:[1,0]
	v_pk_mul_f32 v[4:5], v[4:5], v[34:35] op_sel_hi:[1,0]
	v_cvt_pk_bf16_f32 v2, v2, v3
	v_cvt_pk_bf16_f32 v3, v4, v5
	v_pk_mul_f32 v[4:5], v[6:7], v[34:35] op_sel_hi:[1,0]
	v_pk_mul_f32 v[6:7], v[8:9], v[34:35] op_sel_hi:[1,0]
	v_lshl_add_u64 v[36:37], v[36:37], 0, s[4:5]
	v_lshlrev_b32_e32 v98, 1, v35
	v_cvt_pk_bf16_f32 v4, v4, v5
	v_cvt_pk_bf16_f32 v5, v6, v7
	v_lshl_add_u64 v[36:37], v[36:37], 0, v[98:99]
	v_permlane32_swap_b32_e32 v2, v4
	v_permlane32_swap_b32_e32 v3, v5
	global_store_dwordx4 v[36:37], v[2:5], off
	v_pk_mul_f32 v[6:7], v[16:17], v[34:35] op_sel_hi:[1,0]
	s_addk_i32 s87, 0x100
	v_pk_mul_f32 v[2:3], v[10:11], v[34:35] op_sel_hi:[1,0]
	v_pk_mul_f32 v[4:5], v[12:13], v[34:35] op_sel_hi:[1,0]
	v_cvt_pk_bf16_f32 v2, v2, v3
	v_cvt_pk_bf16_f32 v3, v4, v5
	v_pk_mul_f32 v[4:5], v[14:15], v[34:35] op_sel_hi:[1,0]
	s_cmp_ge_u32 s87, s86
	v_cvt_pk_bf16_f32 v4, v4, v5
	v_cvt_pk_bf16_f32 v5, v6, v7
	s_nop 0
	v_permlane32_swap_b32_e32 v2, v4
	v_permlane32_swap_b32_e32 v3, v5
	global_store_dwordx4 v[36:37], v[2:5], off offset:32
	v_pk_mul_f32 v[6:7], v[24:25], v[34:35] op_sel_hi:[1,0]
	s_nop 0
	v_pk_mul_f32 v[2:3], v[18:19], v[34:35] op_sel_hi:[1,0]
	v_pk_mul_f32 v[4:5], v[20:21], v[34:35] op_sel_hi:[1,0]
	v_cvt_pk_bf16_f32 v2, v2, v3
	v_cvt_pk_bf16_f32 v3, v4, v5
	v_pk_mul_f32 v[4:5], v[22:23], v[34:35] op_sel_hi:[1,0]
	s_nop 0
	v_cvt_pk_bf16_f32 v4, v4, v5
	v_cvt_pk_bf16_f32 v5, v6, v7
	s_nop 0
	v_permlane32_swap_b32_e32 v2, v4
	v_permlane32_swap_b32_e32 v3, v5
	global_store_dwordx4 v[36:37], v[2:5], off offset:64
	v_pk_mul_f32 v[6:7], v[32:33], v[34:35] op_sel_hi:[1,0]
	s_nop 0
	v_pk_mul_f32 v[2:3], v[26:27], v[34:35] op_sel_hi:[1,0]
	v_pk_mul_f32 v[4:5], v[28:29], v[34:35] op_sel_hi:[1,0]
	v_cvt_pk_bf16_f32 v2, v2, v3
	v_cvt_pk_bf16_f32 v3, v4, v5
	v_pk_mul_f32 v[4:5], v[30:31], v[34:35] op_sel_hi:[1,0]
	s_nop 0
	v_cvt_pk_bf16_f32 v4, v4, v5
	v_cvt_pk_bf16_f32 v5, v6, v7
	s_nop 0
	v_permlane32_swap_b32_e32 v2, v4
	v_permlane32_swap_b32_e32 v3, v5
	global_store_dwordx4 v[36:37], v[2:5], off offset:96
	s_cbranch_scc1 .LBB0_1679

.LBB0_1598:
	ds_read_b128 v[36:39], v211 offset:12288
	ds_read_b128 v[52:55], v211 offset:12320
	ds_read_b128 v[56:59], v211 offset:18432
	ds_read_b128 v[60:63], v211 offset:18464
	v_exp_f32_e32 v84, v116
	v_exp_f32_e32 v98, v132
	s_waitcnt lgkmcnt(0)
	v_mfma_f32_32x32x16_bf16 v[36:51], v[36:39], v[168:171], 0
	v_exp_f32_e32 v85, v117
	v_exp_f32_e32 v116, v133
	v_exp_f32_e32 v117, v118
	v_exp_f32_e32 v118, v134
	v_exp_f32_e32 v125, v125
	v_exp_f32_e32 v132, v141
	v_exp_f32_e32 v129, v129
	v_mfma_f32_32x32x16_bf16 v[68:83], v[56:59], v[168:171], 0
	v_cvt_pk_bf16_f32 v84, v84, v85
	v_mfma_f32_32x32x16_bf16 v[36:51], v[52:55], v[148:151], v[36:51]
	ds_read_b128 v[52:55], v211 offset:12352
	ds_read_b128 v[56:59], v211 offset:12384
	v_mfma_f32_32x32x16_bf16 v[68:83], v[60:63], v[148:151], v[68:83]
	v_exp_f32_e32 v61, v126
	v_exp_f32_e32 v126, v142
	v_exp_f32_e32 v62, v127
	v_exp_f32_e32 v127, v143
	v_exp_f32_e32 v63, v128
	v_exp_f32_e32 v128, v144
	v_cvt_pk_bf16_f32 v61, v61, v62
	s_waitcnt lgkmcnt(0)
	v_mfma_f32_32x32x16_bf16 v[36:51], v[52:55], v[152:155], v[36:51]
	ds_read_b128 v[52:55], v211 offset:18496
	ds_read_b128 v[86:89], v211 offset:18528
	ds_read_b128 v[90:93], v226 offset:12288
	ds_read_b128 v[94:97], v226 offset:18432
	v_cvt_pk_bf16_f32 v62, v63, v129
	s_waitcnt lgkmcnt(0)
	v_mfma_f32_32x32x16_bf16 v[68:83], v[52:55], v[152:155], v[68:83]
	v_exp_f32_e32 v54, v145
	v_exp_f32_e32 v52, v130
	v_exp_f32_e32 v55, v146
	v_exp_f32_e32 v53, v131
	v_exp_f32_e32 v130, v147
	v_cvt_pk_bf16_f32 v54, v128, v54
	v_cvt_pk_bf16_f32 v63, v52, v53
	v_mfma_f32_32x32x16_bf16 v[36:51], v[56:59], v[156:159], v[36:51]
	ds_read_b128 v[56:59], v227 offset:12288
	ds_read_b128 v[236:239], v227 offset:18432
	v_cvt_pk_bf16_f32 v53, v126, v127
	v_cvt_pk_bf16_f32 v55, v55, v130
	v_mfma_f32_32x32x16_bf16 v[68:83], v[86:89], v[156:159], v[68:83]
	v_mfma_f32_32x32x16_bf16 v[36:51], v[90:93], v[160:163], v[36:51]
	v_exp_f32_e32 v90, v119
	v_exp_f32_e32 v91, v135
	v_exp_f32_e32 v92, v120
	v_exp_f32_e32 v93, v136
	v_exp_f32_e32 v119, v121
	v_exp_f32_e32 v120, v137
	v_exp_f32_e32 v121, v122
	v_mfma_f32_32x32x16_bf16 v[68:83], v[94:97], v[160:163], v[68:83]
	v_exp_f32_e32 v122, v139
	v_cvt_pk_bf16_f32 v85, v117, v90
	v_cvt_pk_bf16_f32 v86, v92, v119
	s_waitcnt lgkmcnt(0)
	v_mfma_f32_32x32x16_bf16 v[36:51], v[56:59], v[164:167], v[36:51]
	v_exp_f32_e32 v59, v138
	v_exp_f32_e32 v56, v123
	v_exp_f32_e32 v123, v124
	v_exp_f32_e32 v124, v140
	v_cvt_pk_bf16_f32 v57, v118, v91
	v_cvt_pk_bf16_f32 v87, v121, v56
	v_cvt_pk_bf16_f32 v56, v98, v116
	v_mfma_f32_32x32x16_bf16 v[68:83], v[236:239], v[164:167], v[68:83]
	v_cvt_pk_bf16_f32 v58, v93, v120
	v_cvt_pk_bf16_f32 v59, v59, v122
	v_cvt_pk_bf16_f32 v60, v123, v125
	v_cvt_pk_bf16_f32 v52, v124, v132
	v_max3_f32 v96, v36, v37, v68
	v_max_f32_e32 v97, v51, v51
	v_max3_f32 v96, v96, v69, v38
	ds_read_b64_tr_b16 v[120:121], v234 offset:0
	ds_read_b64_tr_b16 v[122:123], v234 offset:1024
	s_nop 0
	v_mfma_f32_4x4x4_16b_bf16 v[100:103], v[240:241], v[84:85], v[100:103]
	v_mfma_f32_4x4x4_16b_bf16 v[104:107], v[240:241], v[86:87], v[104:107]
	v_max3_f32 v96, v96, v70, v71
	ds_read_b64_tr_b16 v[116:117], v235 offset:0
	ds_read_b64_tr_b16 v[118:119], v235 offset:1024
	ds_read_b64_tr_b16 v[92:93], v234 offset:2048
	ds_read_b64_tr_b16 v[94:95], v234 offset:3072
	ds_read_b64_tr_b16 v[88:89], v235 offset:2048
	s_nop 0
	v_max3_f32 v96, v96, v39, v40
	v_mfma_f32_4x4x4_16b_bf16 v[108:111], v[240:241], v[60:61], v[108:111]
	v_mfma_f32_4x4x4_16b_bf16 v[112:115], v[240:241], v[62:63], v[112:115]
	v_max3_f32 v96, v96, v72, v73
	ds_read_b64_tr_b16 v[90:91], v235 offset:3072
	s_nop 0
	v_max3_f32 v96, v96, v41, v42
	v_max3_f32 v96, v96, v74, v75
	v_max3_f32 v96, v96, v43, v44
	v_mfma_f32_4x4x4_16b_bf16 v[100:103], v[240:241], v[56:57], v[100:103]
	v_mfma_f32_4x4x4_16b_bf16 v[104:107], v[240:241], v[58:59], v[104:107]
	v_max3_f32 v96, v96, v76, v77
	v_max3_f32 v96, v96, v45, v46
	v_max3_f32 v96, v96, v78, v79
	v_max3_f32 v96, v96, v47, v48
	v_mfma_f32_4x4x4_16b_bf16 v[108:111], v[240:241], v[52:53], v[108:111]
	v_mfma_f32_4x4x4_16b_bf16 v[112:115], v[240:241], v[54:55], v[112:115]
	v_max3_f32 v96, v96, v80, v81
	v_max3_f32 v96, v96, v49, v50
	v_max3_f32 v96, v96, v82, v83
	v_max_f32_e32 v96, v96, v96
	v_max_f32_e32 v96, v96, v97
	v_mov_b32_e32 v97, v96
	s_nop 1
	v_permlane32_swap_b32_e32 v96, v97
	v_sub_f32_e32 v96, v96, v66
	s_waitcnt lgkmcnt(0)
	s_nop 0
	v_mfma_f32_32x32x16_bf16 v[2:17], v[120:123], v[84:87], v[2:17]
	v_mfma_f32_32x32x16_bf16 v[18:33], v[116:119], v[84:87], v[18:33]
	v_mfma_f32_32x32x16_bf16 v[2:17], v[92:95], v[60:63], v[2:17]
	v_mfma_f32_32x32x16_bf16 v[18:33], v[88:91], v[60:63], v[18:33]
	ds_read_b64_tr_b16 v[60:61], v234 offset:4096
	ds_read_b64_tr_b16 v[62:63], v234 offset:5120
	ds_read_b64_tr_b16 v[84:85], v235 offset:4096
	ds_read_b64_tr_b16 v[86:87], v235 offset:5120
	ds_read_b64_tr_b16 v[88:89], v234 offset:6144
	ds_read_b64_tr_b16 v[90:91], v234 offset:7168
	ds_read_b64_tr_b16 v[92:93], v235 offset:6144
	ds_read_b64_tr_b16 v[94:95], v235 offset:7168
	s_nop 0
	s_waitcnt lgkmcnt(0)
	s_nop 0
	v_mfma_f32_32x32x16_bf16 v[2:17], v[60:63], v[56:59], v[2:17]
	v_mfma_f32_32x32x16_bf16 v[18:33], v[84:87], v[56:59], v[18:33]
	v_mfma_f32_32x32x16_bf16 v[2:17], v[88:91], v[52:55], v[2:17]
	v_mfma_f32_32x32x16_bf16 v[18:33], v[92:95], v[52:55], v[18:33]
	v_cmp_lt_f32_e32 vcc, s29, v96
	s_cbranch_vccz .LBB0_1600
	v_max_f32_e32 v52, v96, v96
	v_max_f32_e32 v53, 0, v52
	v_exp_f32_e64 v52, -v53
	v_add_f32_e32 v66, v66, v53
	v_mul_f32_e32 v34, v34, v52
	v_pk_mul_f32 v[114:115], v[114:115], v[52:53] op_sel_hi:[1,0]
	v_pk_mul_f32 v[112:113], v[112:113], v[52:53] op_sel_hi:[1,0]
	v_pk_mul_f32 v[110:111], v[110:111], v[52:53] op_sel_hi:[1,0]
	v_pk_mul_f32 v[108:109], v[108:109], v[52:53] op_sel_hi:[1,0]
	v_pk_mul_f32 v[106:107], v[106:107], v[52:53] op_sel_hi:[1,0]
	v_pk_mul_f32 v[104:105], v[104:105], v[52:53] op_sel_hi:[1,0]
	v_pk_mul_f32 v[102:103], v[102:103], v[52:53] op_sel_hi:[1,0]
	v_pk_mul_f32 v[100:101], v[100:101], v[52:53] op_sel_hi:[1,0]
	v_pk_mul_f32 v[32:33], v[52:53], v[32:33] op_sel_hi:[0,1]
	v_pk_mul_f32 v[30:31], v[52:53], v[30:31] op_sel_hi:[0,1]
	v_pk_mul_f32 v[28:29], v[52:53], v[28:29] op_sel_hi:[0,1]
	v_pk_mul_f32 v[26:27], v[52:53], v[26:27] op_sel_hi:[0,1]
	v_pk_mul_f32 v[24:25], v[52:53], v[24:25] op_sel_hi:[0,1]
	v_pk_mul_f32 v[22:23], v[52:53], v[22:23] op_sel_hi:[0,1]
	v_pk_mul_f32 v[20:21], v[52:53], v[20:21] op_sel_hi:[0,1]
	v_pk_mul_f32 v[18:19], v[52:53], v[18:19] op_sel_hi:[0,1]
	v_pk_mul_f32 v[16:17], v[52:53], v[16:17] op_sel_hi:[0,1]
	v_pk_mul_f32 v[14:15], v[52:53], v[14:15] op_sel_hi:[0,1]
	v_pk_mul_f32 v[12:13], v[52:53], v[12:13] op_sel_hi:[0,1]
	v_pk_mul_f32 v[10:11], v[52:53], v[10:11] op_sel_hi:[0,1]
	v_pk_mul_f32 v[8:9], v[52:53], v[8:9] op_sel_hi:[0,1]
	v_pk_mul_f32 v[6:7], v[52:53], v[6:7] op_sel_hi:[0,1]
	v_pk_mul_f32 v[4:5], v[52:53], v[4:5] op_sel_hi:[0,1]
	v_pk_mul_f32 v[2:3], v[52:53], v[2:3] op_sel_hi:[0,1]

.LBB0_1631:
	s_mov_b32 s31, s89
	ds_read_b128 v[52:55], v211
	ds_read_b128 v[56:59], v211 offset:32
	v_exp_f32_e32 v36, v36
	v_exp_f32_e32 v68, v68
	v_exp_f32_e32 v37, v37
	s_waitcnt lgkmcnt(0)
	v_mfma_f32_32x32x16_bf16 v[116:131], v[52:55], v[168:171], 0
	ds_read_b128 v[52:55], v211 offset:6144
	ds_read_b128 v[60:63], v211 offset:6176
	v_exp_f32_e32 v69, v69
	v_exp_f32_e32 v38, v38
	v_exp_f32_e32 v70, v70
	v_exp_f32_e32 v39, v39
	v_exp_f32_e32 v71, v71
	v_exp_f32_e32 v40, v40
	s_waitcnt lgkmcnt(0)
	v_mfma_f32_32x32x16_bf16 v[132:147], v[52:55], v[168:171], 0
	v_exp_f32_e32 v72, v72
	v_exp_f32_e32 v41, v41
	v_exp_f32_e32 v73, v73
	v_exp_f32_e32 v42, v42
	v_exp_f32_e32 v43, v43
	v_exp_f32_e32 v44, v44
	v_exp_f32_e32 v45, v45
	v_mfma_f32_32x32x16_bf16 v[116:131], v[56:59], v[148:151], v[116:131]
	ds_read_b128 v[52:55], v211 offset:64
	ds_read_b128 v[56:59], v211 offset:96
	v_exp_f32_e32 v46, v46
	v_exp_f32_e32 v47, v47
	v_cvt_pk_bf16_f32 v44, v44, v45
	v_cvt_pk_bf16_f32 v45, v46, v47
	v_mfma_f32_32x32x16_bf16 v[132:147], v[60:63], v[148:151], v[132:147]
	v_exp_f32_e32 v60, v78
	v_exp_f32_e32 v61, v79
	v_exp_f32_e32 v62, v48
	v_exp_f32_e32 v63, v80
	v_cvt_pk_bf16_f32 v48, v36, v37
	v_cvt_pk_bf16_f32 v37, v60, v61
	s_waitcnt lgkmcnt(0)
	v_mfma_f32_32x32x16_bf16 v[116:131], v[52:55], v[152:155], v[116:131]
	ds_read_b128 v[52:55], v211 offset:6208
	ds_read_b128 v[84:87], v211 offset:6240
	ds_read_b128 v[88:91], v226
	ds_read_b128 v[92:95], v226 offset:6144
	s_waitcnt lgkmcnt(0)
	v_mfma_f32_32x32x16_bf16 v[132:147], v[52:55], v[152:155], v[132:147]
	v_exp_f32_e32 v52, v81
	v_exp_f32_e32 v53, v50
	v_exp_f32_e32 v54, v82
	v_exp_f32_e32 v55, v51
	v_cvt_pk_bf16_f32 v50, v40, v41
	v_cvt_pk_bf16_f32 v51, v42, v43
	v_cvt_pk_bf16_f32 v40, v68, v69
	v_mfma_f32_32x32x16_bf16 v[116:131], v[56:59], v[156:159], v[116:131]
	ds_read_b128 v[56:59], v227
	ds_read_b128 v[236:239], v227 offset:6144
	v_cvt_pk_bf16_f32 v41, v70, v71
	v_cvt_pk_bf16_f32 v42, v72, v73
	v_cvt_pk_bf16_f32 v47, v53, v55
	v_mfma_f32_32x32x16_bf16 v[132:147], v[84:87], v[156:159], v[132:147]
	v_mfma_f32_32x32x16_bf16 v[116:131], v[88:91], v[160:163], v[116:131]
	v_mfma_f32_32x32x16_bf16 v[132:147], v[92:95], v[160:163], v[132:147]
	s_waitcnt lgkmcnt(0)
	v_mfma_f32_32x32x16_bf16 v[116:131], v[56:59], v[164:167], v[116:131]
	v_exp_f32_e32 v56, v74
	v_exp_f32_e32 v57, v75
	v_exp_f32_e32 v58, v76
	v_exp_f32_e32 v59, v77
	v_exp_f32_e32 v74, v49
	v_exp_f32_e32 v75, v83
	v_cvt_pk_bf16_f32 v49, v38, v39
	v_mfma_f32_32x32x16_bf16 v[132:147], v[236:239], v[164:167], v[132:147]
	v_cvt_pk_bf16_f32 v43, v56, v57
	v_cvt_pk_bf16_f32 v46, v62, v74
	v_cvt_pk_bf16_f32 v36, v58, v59
	v_cvt_pk_bf16_f32 v38, v63, v52
	v_cvt_pk_bf16_f32 v39, v54, v75
	v_max3_f32 v72, v116, v117, v132
	v_max_f32_e32 v73, v131, v131
	v_max3_f32 v72, v72, v133, v118
	ds_read_b64_tr_b16 v[68:69], v205 offset:0
	ds_read_b64_tr_b16 v[70:71], v205 offset:1024
	s_nop 0
	v_mfma_f32_4x4x4_16b_bf16 v[100:103], v[240:241], v[48:49], v[100:103]
	v_mfma_f32_4x4x4_16b_bf16 v[104:107], v[240:241], v[50:51], v[104:107]
	v_max3_f32 v72, v72, v134, v135
	ds_read_b64_tr_b16 v[60:61], v67 offset:0
	ds_read_b64_tr_b16 v[62:63], v67 offset:1024
	ds_read_b64_tr_b16 v[56:57], v205 offset:2048
	ds_read_b64_tr_b16 v[58:59], v205 offset:3072
	ds_read_b64_tr_b16 v[52:53], v67 offset:2048
	s_nop 0
	v_max3_f32 v72, v72, v119, v120
	v_mfma_f32_4x4x4_16b_bf16 v[108:111], v[240:241], v[44:45], v[108:111]
	v_mfma_f32_4x4x4_16b_bf16 v[112:115], v[240:241], v[46:47], v[112:115]
	v_max3_f32 v72, v72, v136, v137
	ds_read_b64_tr_b16 v[54:55], v67 offset:3072
	s_nop 0
	v_max3_f32 v72, v72, v121, v122
	v_max3_f32 v72, v72, v138, v139
	v_max3_f32 v72, v72, v123, v124
	v_mfma_f32_4x4x4_16b_bf16 v[100:103], v[240:241], v[40:41], v[100:103]
	v_mfma_f32_4x4x4_16b_bf16 v[104:107], v[240:241], v[42:43], v[104:107]
	v_max3_f32 v72, v72, v140, v141
	v_max3_f32 v72, v72, v125, v126
	v_max3_f32 v72, v72, v142, v143
	v_max3_f32 v72, v72, v127, v128
	v_mfma_f32_4x4x4_16b_bf16 v[108:111], v[240:241], v[36:37], v[108:111]
	v_mfma_f32_4x4x4_16b_bf16 v[112:115], v[240:241], v[38:39], v[112:115]
	v_max3_f32 v72, v72, v144, v145
	v_max3_f32 v72, v72, v129, v130
	v_max3_f32 v72, v72, v146, v147
	v_max_f32_e32 v72, v72, v72
	v_max_f32_e32 v72, v72, v73
	v_mov_b32_e32 v73, v72
	s_nop 1
	v_permlane32_swap_b32_e32 v72, v73
	v_sub_f32_e32 v72, v72, v66
	s_waitcnt lgkmcnt(0)
	s_nop 0
	v_mfma_f32_32x32x16_bf16 v[2:17], v[68:71], v[48:51], v[2:17]
	v_mfma_f32_32x32x16_bf16 v[18:33], v[60:63], v[48:51], v[18:33]
	v_mfma_f32_32x32x16_bf16 v[2:17], v[56:59], v[44:47], v[2:17]
	v_mfma_f32_32x32x16_bf16 v[18:33], v[52:55], v[44:47], v[18:33]
	ds_read_b64_tr_b16 v[44:45], v205 offset:4096
	ds_read_b64_tr_b16 v[46:47], v205 offset:5120
	ds_read_b64_tr_b16 v[48:49], v67 offset:4096
	ds_read_b64_tr_b16 v[50:51], v67 offset:5120
	ds_read_b64_tr_b16 v[52:53], v205 offset:6144
	ds_read_b64_tr_b16 v[54:55], v205 offset:7168
	ds_read_b64_tr_b16 v[56:57], v67 offset:6144
	ds_read_b64_tr_b16 v[58:59], v67 offset:7168
	s_nop 0
	s_waitcnt lgkmcnt(0)
	s_nop 0
	v_mfma_f32_32x32x16_bf16 v[2:17], v[44:47], v[40:43], v[2:17]
	v_mfma_f32_32x32x16_bf16 v[18:33], v[48:51], v[40:43], v[18:33]
	v_mfma_f32_32x32x16_bf16 v[2:17], v[52:55], v[36:39], v[2:17]
	v_mfma_f32_32x32x16_bf16 v[18:33], v[56:59], v[36:39], v[18:33]
	v_cmp_lt_f32_e32 vcc, s29, v72
	s_cbranch_vccz .LBB0_1633
	v_max_f32_e32 v36, v72, v72
	v_max_f32_e32 v37, 0, v36
	v_exp_f32_e64 v36, -v37
	v_add_f32_e32 v66, v66, v37
	v_mul_f32_e32 v34, v34, v36
	v_pk_mul_f32 v[114:115], v[114:115], v[36:37] op_sel_hi:[1,0]
	v_pk_mul_f32 v[112:113], v[112:113], v[36:37] op_sel_hi:[1,0]
	v_pk_mul_f32 v[110:111], v[110:111], v[36:37] op_sel_hi:[1,0]
	v_pk_mul_f32 v[108:109], v[108:109], v[36:37] op_sel_hi:[1,0]
	v_pk_mul_f32 v[106:107], v[106:107], v[36:37] op_sel_hi:[1,0]
	v_pk_mul_f32 v[104:105], v[104:105], v[36:37] op_sel_hi:[1,0]
	v_pk_mul_f32 v[102:103], v[102:103], v[36:37] op_sel_hi:[1,0]
	v_pk_mul_f32 v[100:101], v[100:101], v[36:37] op_sel_hi:[1,0]
	v_pk_mul_f32 v[32:33], v[36:37], v[32:33] op_sel_hi:[0,1]
	v_pk_mul_f32 v[30:31], v[36:37], v[30:31] op_sel_hi:[0,1]
	v_pk_mul_f32 v[28:29], v[36:37], v[28:29] op_sel_hi:[0,1]
	v_pk_mul_f32 v[26:27], v[36:37], v[26:27] op_sel_hi:[0,1]
	v_pk_mul_f32 v[24:25], v[36:37], v[24:25] op_sel_hi:[0,1]
	v_pk_mul_f32 v[22:23], v[36:37], v[22:23] op_sel_hi:[0,1]
	v_pk_mul_f32 v[20:21], v[36:37], v[20:21] op_sel_hi:[0,1]
	v_pk_mul_f32 v[18:19], v[36:37], v[18:19] op_sel_hi:[0,1]
	v_pk_mul_f32 v[16:17], v[36:37], v[16:17] op_sel_hi:[0,1]
	v_pk_mul_f32 v[14:15], v[36:37], v[14:15] op_sel_hi:[0,1]
	v_pk_mul_f32 v[12:13], v[36:37], v[12:13] op_sel_hi:[0,1]
	v_pk_mul_f32 v[10:11], v[36:37], v[10:11] op_sel_hi:[0,1]
	v_pk_mul_f32 v[8:9], v[36:37], v[8:9] op_sel_hi:[0,1]
	v_pk_mul_f32 v[6:7], v[36:37], v[6:7] op_sel_hi:[0,1]
	v_pk_mul_f32 v[4:5], v[36:37], v[4:5] op_sel_hi:[0,1]
	v_pk_mul_f32 v[2:3], v[36:37], v[2:3] op_sel_hi:[0,1]

.LBB0_1666:
	s_bitcmp1_b32 s11, 0
	s_cselect_b32 s4, 0x3000, 0
	s_add_i32 s4, s4, 0
	v_add_u32_e32 v92, s4, v207
	ds_read_b128 v[36:39], v92
	ds_read_b128 v[52:55], v92 offset:32
	v_add3_u32 v64, v207, v208, s4
	v_exp_f32_e32 v93, v116
	v_exp_f32_e32 v94, v117
	s_waitcnt lgkmcnt(0)
	v_mfma_f32_32x32x16_bf16 v[68:83], v[36:39], v[168:171], 0
	ds_read_b128 v[36:39], v92 offset:6144
	ds_read_b128 v[56:59], v92 offset:6176
	ds_read_b128 v[60:63], v92 offset:96
	v_exp_f32_e32 v95, v118
	v_exp_f32_e32 v96, v119
	v_exp_f32_e32 v97, v120
	v_exp_f32_e32 v98, v121
	v_add3_u32 v88, v207, v206, s4
	v_mfma_f32_32x32x16_bf16 v[68:83], v[52:55], v[148:151], v[68:83]
	ds_read_b128 v[52:55], v92 offset:64
	v_exp_f32_e32 v174, v128
	v_exp_f32_e32 v175, v129
	v_exp_f32_e32 v176, v130
	v_exp_f32_e32 v177, v131
	s_waitcnt lgkmcnt(0)
	v_mfma_f32_32x32x16_bf16 v[36:51], v[36:39], v[168:171], 0
	v_exp_f32_e32 v168, v122
	v_exp_f32_e32 v169, v125
	v_exp_f32_e32 v170, v126
	v_exp_f32_e32 v171, v127
	v_mfma_f32_32x32x16_bf16 v[68:83], v[52:55], v[152:155], v[68:83]
	ds_read_b128 v[52:55], v64
	v_mfma_f32_32x32x16_bf16 v[68:83], v[60:63], v[156:159], v[68:83]
	v_exp_f32_e32 v60, v123
	v_exp_f32_e32 v61, v124
	ds_read_b128 v[62:65], v64 offset:6144
	ds_read_b128 v[84:87], v88
	ds_read_b128 v[88:91], v88 offset:6144
	s_waitcnt lgkmcnt(0)
	v_mfma_f32_32x32x16_bf16 v[68:83], v[52:55], v[160:163], v[68:83]
	v_mfma_f32_32x32x16_bf16 v[36:51], v[56:59], v[148:151], v[36:51]
	s_nop 10
	v_mov_b64_e32 v[130:131], v[82:83]
	v_mov_b64_e32 v[128:129], v[80:81]
	v_mov_b64_e32 v[126:127], v[78:79]
	v_mov_b64_e32 v[124:125], v[76:77]
	v_mov_b64_e32 v[122:123], v[74:75]
	v_mov_b64_e32 v[120:121], v[72:73]
	v_mov_b64_e32 v[118:119], v[70:71]
	v_mov_b64_e32 v[116:117], v[68:69]
	ds_read_b128 v[52:55], v92 offset:6208
	ds_read_b128 v[72:75], v92 offset:6240
	s_waitcnt lgkmcnt(0)
	v_mfma_f32_32x32x16_bf16 v[36:51], v[52:55], v[152:155], v[36:51]
	v_exp_f32_e32 v76, v132
	v_exp_f32_e32 v77, v133
	v_exp_f32_e32 v78, v134
	v_exp_f32_e32 v79, v135
	v_exp_f32_e32 v80, v136
	v_exp_f32_e32 v58, v137
	v_exp_f32_e32 v59, v138
	v_mfma_f32_32x32x16_bf16 v[36:51], v[72:75], v[156:159], v[36:51]
	v_exp_f32_e32 v81, v139
	v_exp_f32_e32 v82, v140
	v_exp_f32_e32 v83, v141
	v_exp_f32_e32 v54, v144
	v_exp_f32_e32 v55, v145
	v_cvt_pk_bf16_f32 v68, v93, v94
	v_cvt_pk_bf16_f32 v69, v95, v96
	v_mfma_f32_32x32x16_bf16 v[36:51], v[62:65], v[160:163], v[36:51]
	v_cvt_pk_bf16_f32 v70, v97, v98
	v_cvt_pk_bf16_f32 v71, v168, v60
	v_cvt_pk_bf16_f32 v56, v76, v77
	v_cvt_pk_bf16_f32 v57, v78, v79
	v_cvt_pk_bf16_f32 v58, v80, v58
	v_cvt_pk_bf16_f32 v59, v59, v81
	v_cvt_pk_bf16_f32 v60, v61, v169
	v_mfma_f32_32x32x16_bf16 v[116:131], v[84:87], v[164:167], v[116:131]
	v_exp_f32_e32 v84, v142
	v_exp_f32_e32 v85, v143
	v_exp_f32_e32 v86, v146
	v_exp_f32_e32 v87, v147
	v_mov_b64_e32 v[146:147], v[50:51]
	v_mov_b64_e32 v[144:145], v[48:49]
	v_mov_b64_e32 v[142:143], v[46:47]
	v_mov_b64_e32 v[140:141], v[44:45]
	v_mov_b64_e32 v[138:139], v[42:43]
	v_mov_b64_e32 v[136:137], v[40:41]
	v_mov_b64_e32 v[134:135], v[38:39]
	v_mov_b64_e32 v[132:133], v[36:37]
	v_cvt_pk_bf16_f32 v61, v170, v171
	v_cvt_pk_bf16_f32 v62, v174, v175
	v_mfma_f32_32x32x16_bf16 v[132:147], v[88:91], v[164:167], v[132:147]
	v_cvt_pk_bf16_f32 v63, v176, v177
	v_cvt_pk_bf16_f32 v52, v82, v83
	v_cvt_pk_bf16_f32 v53, v84, v85
	v_cvt_pk_bf16_f32 v54, v54, v55
	v_cvt_pk_bf16_f32 v55, v86, v87
	v_mov_b64_e32 v[74:75], s[92:93]
	v_mov_b64_e32 v[76:77], s[94:95]
	v_max3_f32 v72, v116, v117, v132
	s_not_b32 s4, s11
	v_max3_f32 v72, v72, v133, v118
	s_lshl_b32 s4, s4, 13
	v_mfma_f32_4x4x4_16b_bf16 v[100:103], v[74:75], v[68:69], v[100:103]
	v_mfma_f32_4x4x4_16b_bf16 v[104:107], v[74:75], v[70:71], v[104:107]
	v_max3_f32 v72, v72, v134, v135
	v_max_f32_e32 v73, v131, v131
	v_max3_f32 v72, v72, v119, v120
	s_and_b32 s4, s4, 0x2000
	v_max3_f32 v72, v72, v136, v137
	s_add_i32 s4, s4, 0
	v_max3_f32 v72, v72, v121, v122
	v_mfma_f32_4x4x4_16b_bf16 v[108:111], v[74:75], v[60:61], v[108:111]
	v_mfma_f32_4x4x4_16b_bf16 v[112:115], v[74:75], v[62:63], v[112:115]
	v_max3_f32 v72, v72, v138, v139
	s_addk_i32 s4, 0x6000
	v_max3_f32 v72, v72, v123, v124
	v_add_u32_e32 v64, s4, v209
	v_max3_f32 v72, v72, v140, v141
	v_add_u32_e32 v65, s4, v210
	v_max3_f32 v72, v72, v125, v126
	v_mfma_f32_4x4x4_16b_bf16 v[100:103], v[74:75], v[56:57], v[100:103]
	v_mfma_f32_4x4x4_16b_bf16 v[104:107], v[74:75], v[58:59], v[104:107]
	v_max3_f32 v72, v72, v142, v143
	ds_read_b64_tr_b16 v[48:49], v64 offset:0
	ds_read_b64_tr_b16 v[50:51], v64 offset:1024
	ds_read_b64_tr_b16 v[44:45], v65 offset:0
	ds_read_b64_tr_b16 v[46:47], v65 offset:1024
	ds_read_b64_tr_b16 v[40:41], v64 offset:2048
	s_nop 0
	v_max3_f32 v72, v72, v127, v128
	ds_read_b64_tr_b16 v[42:43], v64 offset:3072
	ds_read_b64_tr_b16 v[36:37], v65 offset:2048
	ds_read_b64_tr_b16 v[38:39], v65 offset:3072
	v_mfma_f32_4x4x4_16b_bf16 v[108:111], v[74:75], v[52:53], v[108:111]
	v_mfma_f32_4x4x4_16b_bf16 v[112:115], v[74:75], v[54:55], v[112:115]
	v_max3_f32 v72, v72, v144, v145
	s_nop 0
	v_max3_f32 v72, v72, v129, v130
	s_nop 0
	v_max3_f32 v72, v72, v146, v147
	s_nop 0
	v_max_f32_e32 v72, v72, v72
	v_max_f32_e32 v72, v72, v73
	v_mov_b32_e32 v73, v72
	s_nop 1
	v_permlane32_swap_b32_e32 v72, v73
	v_sub_f32_e32 v72, v72, v66
	s_waitcnt lgkmcnt(0)
	s_nop 0
	v_mfma_f32_32x32x16_bf16 v[2:17], v[48:51], v[68:71], v[2:17]
	v_mfma_f32_32x32x16_bf16 v[18:33], v[44:47], v[68:71], v[18:33]
	v_mfma_f32_32x32x16_bf16 v[2:17], v[40:43], v[60:63], v[2:17]
	v_mfma_f32_32x32x16_bf16 v[18:33], v[36:39], v[60:63], v[18:33]
	ds_read_b64_tr_b16 v[36:37], v64 offset:4096
	ds_read_b64_tr_b16 v[38:39], v64 offset:5120
	ds_read_b64_tr_b16 v[40:41], v65 offset:4096
	ds_read_b64_tr_b16 v[42:43], v65 offset:5120
	ds_read_b64_tr_b16 v[44:45], v64 offset:6144
	ds_read_b64_tr_b16 v[46:47], v64 offset:7168
	ds_read_b64_tr_b16 v[48:49], v65 offset:6144
	ds_read_b64_tr_b16 v[50:51], v65 offset:7168
	s_nop 0
	s_waitcnt lgkmcnt(0)
	s_nop 0
	v_mfma_f32_32x32x16_bf16 v[2:17], v[36:39], v[56:59], v[2:17]
	v_mfma_f32_32x32x16_bf16 v[18:33], v[40:43], v[56:59], v[18:33]
	v_mfma_f32_32x32x16_bf16 v[2:17], v[44:47], v[52:55], v[2:17]
	v_mfma_f32_32x32x16_bf16 v[18:33], v[48:51], v[52:55], v[18:33]
	v_cmp_lt_f32_e32 vcc, s29, v72
	s_cbranch_vccz .LBB0_1668
	v_max_f32_e32 v36, v72, v72
	v_max_f32_e32 v37, 0, v36
	v_exp_f32_e64 v36, -v37
	v_add_f32_e32 v66, v66, v37
	v_mul_f32_e32 v34, v34, v36
	v_pk_mul_f32 v[114:115], v[114:115], v[36:37] op_sel_hi:[1,0]
	v_pk_mul_f32 v[112:113], v[112:113], v[36:37] op_sel_hi:[1,0]
	v_pk_mul_f32 v[110:111], v[110:111], v[36:37] op_sel_hi:[1,0]
	v_pk_mul_f32 v[108:109], v[108:109], v[36:37] op_sel_hi:[1,0]
	v_pk_mul_f32 v[106:107], v[106:107], v[36:37] op_sel_hi:[1,0]
	v_pk_mul_f32 v[104:105], v[104:105], v[36:37] op_sel_hi:[1,0]
	v_pk_mul_f32 v[102:103], v[102:103], v[36:37] op_sel_hi:[1,0]
	v_pk_mul_f32 v[100:101], v[100:101], v[36:37] op_sel_hi:[1,0]
	v_pk_mul_f32 v[32:33], v[36:37], v[32:33] op_sel_hi:[0,1]
	v_pk_mul_f32 v[30:31], v[36:37], v[30:31] op_sel_hi:[0,1]
	v_pk_mul_f32 v[28:29], v[36:37], v[28:29] op_sel_hi:[0,1]
	v_pk_mul_f32 v[26:27], v[36:37], v[26:27] op_sel_hi:[0,1]
	v_pk_mul_f32 v[24:25], v[36:37], v[24:25] op_sel_hi:[0,1]
	v_pk_mul_f32 v[22:23], v[36:37], v[22:23] op_sel_hi:[0,1]
	v_pk_mul_f32 v[20:21], v[36:37], v[20:21] op_sel_hi:[0,1]
	v_pk_mul_f32 v[18:19], v[36:37], v[18:19] op_sel_hi:[0,1]
	v_pk_mul_f32 v[16:17], v[36:37], v[16:17] op_sel_hi:[0,1]
	v_pk_mul_f32 v[14:15], v[36:37], v[14:15] op_sel_hi:[0,1]
	v_pk_mul_f32 v[12:13], v[36:37], v[12:13] op_sel_hi:[0,1]
	v_pk_mul_f32 v[10:11], v[36:37], v[10:11] op_sel_hi:[0,1]
	v_pk_mul_f32 v[8:9], v[36:37], v[8:9] op_sel_hi:[0,1]
	v_pk_mul_f32 v[6:7], v[36:37], v[6:7] op_sel_hi:[0,1]
	v_pk_mul_f32 v[4:5], v[36:37], v[4:5] op_sel_hi:[0,1]
	v_pk_mul_f32 v[2:3], v[36:37], v[2:3] op_sel_hi:[0,1]
